# LoRA up-projection loop: weight-fragment loads issued ahead with counted vmcnt waits
# speedup vs baseline: 1.0211x; 1.0072x over previous
; #define LAS __attribute__((address_space(3)))
; __device__ __forceinline__ void lora_phase(LAS unsigned char* lds, const bf16_t* projb, const float* mix, const float* vmix, const bf16_t* Wl_w, const bf16_t* Wl_a, const bf16_t* Wl_g, const bf16_t* Wl_v, ...
;     ...
;             for (int ks = 0; ks < K / 32; ++ks) {
;                 bf16x8 af[8], bfr[4];
; #pragma unroll
;                 for (int ct = 0; ct < 8; ++ct) af[ct] = *(const bf16x8*)(W + (size_t)(128 * wave + 32 * (ct >> 1) + 8 * (fr >> 2) + 4 * (ct & 1) + (fr & 3)) * K + 32 * ks + 8 * fq);
; #pragma unroll
;                 for (int tt = 0; tt < 4; ++tt) bfr[tt] = *(const LAS bf16x8*)(Aimg + (16 * tt + fr) * LORA_PITCH + koff + 32 * ks + 8 * fq);
; #pragma unroll
;                 for (int ct = 0; ct < 8; ++ct)
; #pragma unroll
;                     for (int tt = 0; tt < 4; ++tt) acc[ct][tt] = __builtin_amdgcn_mfma_f32_16x16x32_bf16(af[ct], bfr[tt], acc[ct][tt], 0, 0, 0);
;             }
.LBB0_374:
	v_lshl_add_u64 v[198:199], s[92:93], 1, v[180:181]
	v_lshl_add_u64 v[132:133], v[182:183], 1, v[198:199]
	global_load_dwordx4 v[206:209], v[132:133], off
	ds_read_b128 v[202:205], v2
	ds_read_b128 v[210:213], v2 offset:10496
	ds_read_b128 v[214:217], v2 offset:20992
	ds_read_b128 v[132:135], v2 offset:31488
	v_lshl_add_u64 v[218:219], v[184:185], 1, v[198:199]
	global_load_dwordx4 v[220:223], v[218:219], off
	v_lshl_add_u64 v[218:219], v[186:187], 1, v[198:199]
	global_load_dwordx4 v[224:227], v[218:219], off
	v_lshl_add_u64 v[218:219], v[188:189], 1, v[198:199]
	global_load_dwordx4 v[228:231], v[218:219], off
	v_lshl_add_u64 v[218:219], v[190:191], 1, v[198:199]
	global_load_dwordx4 v[232:235], v[218:219], off
	s_add_i32 s23, s23, -1
	s_add_i32 s92, s92, 32
	s_cmp_eq_u32 s23, 0
	v_add_u32_e32 v2, 64, v2
	s_waitcnt vmcnt(4) lgkmcnt(3)
	v_mfma_f32_16x16x32_bf16 v[128:131], v[206:209], v[202:205], v[128:131]
	s_waitcnt lgkmcnt(2)
	v_mfma_f32_16x16x32_bf16 v[124:127], v[206:209], v[210:213], v[124:127]
	s_waitcnt lgkmcnt(1)
	v_mfma_f32_16x16x32_bf16 v[116:119], v[206:209], v[214:217], v[116:119]
	s_waitcnt lgkmcnt(0)
	v_mfma_f32_16x16x32_bf16 v[108:111], v[206:209], v[132:135], v[108:111]
	v_lshl_add_u64 v[218:219], v[192:193], 1, v[198:199]
	global_load_dwordx4 v[206:209], v[218:219], off
	s_waitcnt vmcnt(4)
	v_mfma_f32_16x16x32_bf16 v[120:123], v[220:223], v[202:205], v[120:123]
	v_mfma_f32_16x16x32_bf16 v[112:115], v[220:223], v[210:213], v[112:115]
	v_mfma_f32_16x16x32_bf16 v[104:107], v[220:223], v[214:217], v[104:107]
	v_mfma_f32_16x16x32_bf16 v[100:103], v[220:223], v[132:135], v[100:103]
	v_lshl_add_u64 v[218:219], v[194:195], 1, v[198:199]
	global_load_dwordx4 v[220:223], v[218:219], off
	s_waitcnt vmcnt(4)
	v_mfma_f32_16x16x32_bf16 v[96:99], v[224:227], v[202:205], v[96:99]
	v_mfma_f32_16x16x32_bf16 v[72:75], v[224:227], v[210:213], v[72:75]
	v_mfma_f32_16x16x32_bf16 v[44:47], v[224:227], v[214:217], v[44:47]
	v_mfma_f32_16x16x32_bf16 v[28:31], v[224:227], v[132:135], v[28:31]
	v_lshl_add_u64 v[218:219], v[196:197], 1, v[198:199]
	global_load_dwordx4 v[224:227], v[218:219], off
	s_waitcnt vmcnt(4)
	v_mfma_f32_16x16x32_bf16 v[60:63], v[228:231], v[202:205], v[60:63]
	v_mfma_f32_16x16x32_bf16 v[36:39], v[228:231], v[210:213], v[36:39]
	v_mfma_f32_16x16x32_bf16 v[24:27], v[228:231], v[214:217], v[24:27]
	v_mfma_f32_16x16x32_bf16 v[20:23], v[228:231], v[132:135], v[20:23]
	s_waitcnt vmcnt(3)
	v_mfma_f32_16x16x32_bf16 v[16:19], v[232:235], v[202:205], v[16:19]
	v_mfma_f32_16x16x32_bf16 v[12:15], v[232:235], v[210:213], v[12:15]
	v_mfma_f32_16x16x32_bf16 v[8:11], v[232:235], v[214:217], v[8:11]
	v_mfma_f32_16x16x32_bf16 v[4:7], v[232:235], v[132:135], v[4:7]
	s_waitcnt vmcnt(2)
	v_mfma_f32_16x16x32_bf16 v[92:95], v[206:209], v[202:205], v[92:95]
	v_mfma_f32_16x16x32_bf16 v[84:87], v[206:209], v[210:213], v[84:87]
	v_mfma_f32_16x16x32_bf16 v[76:79], v[206:209], v[214:217], v[76:79]
	v_mfma_f32_16x16x32_bf16 v[64:67], v[206:209], v[132:135], v[64:67]
	s_waitcnt vmcnt(1)
	v_mfma_f32_16x16x32_bf16 v[56:59], v[220:223], v[202:205], v[56:59]
	v_mfma_f32_16x16x32_bf16 v[48:51], v[220:223], v[210:213], v[48:51]
	v_mfma_f32_16x16x32_bf16 v[40:43], v[220:223], v[214:217], v[40:43]
	v_mfma_f32_16x16x32_bf16 v[32:35], v[220:223], v[132:135], v[32:35]
	s_waitcnt vmcnt(0)
	v_mfma_f32_16x16x32_bf16 v[88:91], v[224:227], v[202:205], v[88:91]
	v_mfma_f32_16x16x32_bf16 v[80:83], v[224:227], v[210:213], v[80:83]
	v_mfma_f32_16x16x32_bf16 v[68:71], v[224:227], v[214:217], v[68:71]
	v_mfma_f32_16x16x32_bf16 v[52:55], v[224:227], v[132:135], v[52:55]
	s_cbranch_scc0 .LBB0_374
; __device__ __forceinline__ unsigned cvt_pk_bf16(float lo, float hi) { const f32x2 v = {lo, hi}; const bf16x2_t b = __builtin_convertvector(v, bf16x2_t); return __builtin_bit_cast(unsigned, b); }
; __device__ __forceinline__ void lora_phase(LAS unsigned char* lds, const bf16_t* projb, const float* mix, const float* vmix, const bf16_t* Wl_w, const bf16_t* Wl_a, const bf16_t* Wl_g, const bf16_t* Wl_v, ...
;     ...
;             bf16_t* out = lw + (size_t)q * M * 1024;
; #pragma unroll
;             for (int cp = 0; cp < 4; ++cp)
; #pragma unroll
;                 for (int tt = 0; tt < 4; ++tt) { u32x4 w; w.x = cvt_pk_bf16(acc[2 * cp][tt][0], acc[2 * cp][tt][1]); w.y = cvt_pk_bf16(acc[2 * cp][tt][2], acc[2 * cp][tt][3]);
;                     w.z = cvt_pk_bf16(acc[2 * cp + 1][tt][0], acc[2 * cp + 1][tt][1]); w.w = cvt_pk_bf16(acc[2 * cp + 1][tt][2], acc[2 * cp + 1][tt][3]);
;                     *(u32x4*)(out + (size_t)(u * 64 + 16 * tt + fr) * 1024 + 128 * wave + 32 * cp + 8 * fq) = w; }
;         }
;         __syncthreads();
;     }
	s_lshl_b32 s92, s22, 25
	s_add_i32 s20, s22, 1
	v_lshl_add_u64 v[132:133], v[140:141], 0, s[92:93]
	s_cmp_gt_u32 s22, 2
	v_cvt_pk_bf16_f32 v128, v128, v129
	v_cvt_pk_bf16_f32 v129, v130, v131
	v_cvt_pk_bf16_f32 v131, v122, v123
	v_cvt_pk_bf16_f32 v123, v114, v115
	v_cvt_pk_bf16_f32 v115, v106, v107
	v_cvt_pk_bf16_f32 v106, v100, v101
	v_lshl_add_u64 v[100:101], v[132:133], 0, v[178:179]
	v_cvt_pk_bf16_f32 v4, v4, v5
	v_cvt_pk_bf16_f32 v5, v6, v7
	v_cvt_pk_bf16_f32 v6, v64, v65
	v_cvt_pk_bf16_f32 v7, v66, v67
	s_cselect_b64 s[22:23], -1, 0
	s_cmp_eq_u32 s20, 3
	v_lshl_add_u64 v[134:135], v[132:133], 0, v[172:173]
	global_store_dwordx4 v[100:101], v[4:7], off offset:128
	s_cselect_b64 s[46:47], -1, 0
	s_xor_b64 s[48:49], s[44:45], -1
	v_cvt_pk_bf16_f32 v4, v56, v57
	v_cvt_pk_bf16_f32 v5, v58, v59
	v_cvt_pk_bf16_f32 v6, v88, v89
	v_cvt_pk_bf16_f32 v7, v90, v91
	v_cvt_pk_bf16_f32 v130, v120, v121
	v_cvt_pk_bf16_f32 v120, v124, v125
	v_lshl_add_u64 v[124:125], v[132:133], 0, v[174:175]
	global_store_dwordx4 v[134:135], v[4:7], off offset:192
	s_and_b64 s[46:47], s[48:49], s[46:47]
	v_cvt_pk_bf16_f32 v122, v112, v113
	v_cvt_pk_bf16_f32 v4, v48, v49
	v_cvt_pk_bf16_f32 v5, v50, v51
	v_cvt_pk_bf16_f32 v6, v80, v81
	v_cvt_pk_bf16_f32 v7, v82, v83
	v_cvt_pk_bf16_f32 v112, v116, v117
	v_lshl_add_u64 v[116:117], v[132:133], 0, v[176:177]
	global_store_dwordx4 v[124:125], v[4:7], off offset:192
	s_or_b64 s[22:23], s[22:23], s[46:47]
	v_cvt_pk_bf16_f32 v121, v126, v127
	v_cvt_pk_bf16_f32 v4, v40, v41
	v_cvt_pk_bf16_f32 v5, v42, v43
	v_cvt_pk_bf16_f32 v6, v68, v69
	v_cvt_pk_bf16_f32 v7, v70, v71
	v_cvt_pk_bf16_f32 v113, v118, v119
	v_cvt_pk_bf16_f32 v114, v104, v105
	v_cvt_pk_bf16_f32 v104, v108, v109
	v_cvt_pk_bf16_f32 v105, v110, v111
	v_cvt_pk_bf16_f32 v107, v102, v103
	v_cvt_pk_bf16_f32 v96, v96, v97
	v_cvt_pk_bf16_f32 v97, v98, v99
	v_cvt_pk_bf16_f32 v98, v60, v61
	v_cvt_pk_bf16_f32 v99, v62, v63
	v_cvt_pk_bf16_f32 v60, v72, v73
	v_cvt_pk_bf16_f32 v61, v74, v75
	v_cvt_pk_bf16_f32 v62, v36, v37
	v_cvt_pk_bf16_f32 v63, v38, v39
	v_cvt_pk_bf16_f32 v36, v44, v45
	v_cvt_pk_bf16_f32 v37, v46, v47
	v_cvt_pk_bf16_f32 v38, v24, v25
	v_cvt_pk_bf16_f32 v39, v26, v27
	v_cvt_pk_bf16_f32 v24, v28, v29
	v_cvt_pk_bf16_f32 v25, v30, v31
	v_cvt_pk_bf16_f32 v26, v20, v21
	v_cvt_pk_bf16_f32 v27, v22, v23
	v_cvt_pk_bf16_f32 v16, v16, v17
	v_cvt_pk_bf16_f32 v17, v18, v19
	v_cvt_pk_bf16_f32 v18, v92, v93
	v_cvt_pk_bf16_f32 v19, v94, v95
	v_cvt_pk_bf16_f32 v12, v12, v13
	v_cvt_pk_bf16_f32 v13, v14, v15
	v_cvt_pk_bf16_f32 v14, v84, v85
	v_cvt_pk_bf16_f32 v15, v86, v87
	v_cvt_pk_bf16_f32 v8, v8, v9
	v_cvt_pk_bf16_f32 v9, v10, v11
	v_cvt_pk_bf16_f32 v10, v76, v77
	v_cvt_pk_bf16_f32 v11, v78, v79
	global_store_dwordx4 v[116:117], v[4:7], off offset:192
	s_and_b64 vcc, exec, s[22:23]
	s_mov_b32 s22, s20
	v_cvt_pk_bf16_f32 v4, v32, v33
	v_cvt_pk_bf16_f32 v5, v34, v35
	v_cvt_pk_bf16_f32 v6, v52, v53
	v_cvt_pk_bf16_f32 v7, v54, v55
	global_store_dwordx4 v[134:135], v[128:131], off
	global_store_dwordx4 v[124:125], v[120:123], off
	global_store_dwordx4 v[116:117], v[112:115], off
	global_store_dwordx4 v[100:101], v[104:107], off
	global_store_dwordx4 v[134:135], v[96:99], off offset:64
	global_store_dwordx4 v[124:125], v[60:63], off offset:64
	global_store_dwordx4 v[116:117], v[36:39], off offset:64
	global_store_dwordx4 v[100:101], v[24:27], off offset:64
	global_store_dwordx4 v[134:135], v[16:19], off offset:128
	global_store_dwordx4 v[124:125], v[12:15], off offset:128
	global_store_dwordx4 v[116:117], v[8:11], off offset:128
	global_store_dwordx4 v[100:101], v[4:7], off offset:192
	s_cbranch_vccz .LBB0_373
	s_add_i32 s50, s50, s60
	s_cmpk_lt_i32 s50, 0x100
	s_barrier
	s_cbranch_scc1 .LBB0_308
	v_readlane_b32 s14, v254, 7
	v_readlane_b32 s15, v254, 8

; __device__ __forceinline__ unsigned xb_ld(unsigned* p)              { return __hip_atomic_load(p, __ATOMIC_RELAXED, __HIP_MEMORY_SCOPE_AGENT); }
; #define XB_SPIN(cond, bar) do { unsigned _sp = 0; while (cond) { __builtin_amdgcn_s_sleep(1); \
;     if ((++_sp & 255u) == 0u) { if (xb_ld(&(bar)[XB_TMO])) break; if (_sp > XB_SPIN_CAP) { atomicAdd(&(bar)[XB_TMO], 1u); break; } } } } while (0)
; __device__ __forceinline__ void xcd_barrier(const XcdBarrier& b) {
;     ...
;             XB_SPIN(xb_ld(&bar[XB_XGEN(b.x)]) == gen, bar);
;             __builtin_amdgcn_fence(__ATOMIC_ACQUIRE, "agent");
;             asm volatile("s_waitcnt vmcnt(0)" ::: "memory");
;         }
.Lxb_spin:
	global_load_dword v6, v3, s[10:11] sc1
	s_waitcnt vmcnt(0)
	v_readfirstlane_b32 s12, v6
	s_cmp_lg_u32 s12, s101
	s_cbranch_scc1 .Lxb_released
	s_sleep 1
	s_add_i32 s13, s13, 1
	s_cmp_lt_u32 s13, 0x100000
	s_cbranch_scc1 .Lxb_spin
